# router phase loop top: row waits recounted so the previous iteration's stores may stay in flight (prefetch is now older than them)
# speedup vs baseline: 1.0049x; 1.0049x over previous
; __device__ __forceinline__ void phase5(Frame& F, const Args& a) {
;     ...
;             f32x4 v[8]; float s = 0.f;
; #pragma unroll
;             for (int j = 0; j < 8; ++j) { const v2u yw = ynx[j]; v[j] = (f32x4){bflo(yw.x), bfhi(yw.x), bflo(yw.y), bfhi(yw.y)}; s += (v[j].x + v[j].y) + (v[j].z + v[j].w); }
;     ...
;         if (sb + 8 < rows_per_wg) {
; #pragma unroll
;             for (int j = 0; j < 8; ++j) ynx[j] = *((const v2u*)(Y1 + (size_t)(m + 8) * D) + lane + 64 * j);
;         }
.LBB0_627:
	s_waitcnt vmcnt(12)
	v_lshlrev_b32_e32 v173, 16, v144
	v_lshlrev_b32_e32 v172, 16, v142
	v_and_b32_e32 v177, 0xffff0000, v144
	v_and_b32_e32 v176, 0xffff0000, v142
	v_lshlrev_b32_e32 v131, 16, v145
	v_lshlrev_b32_e32 v130, 16, v143
	v_and_b32_e32 v133, 0xffff0000, v145
	v_and_b32_e32 v132, 0xffff0000, v143
	v_pk_add_f32 v[134:135], v[172:173], v[176:177]
	v_pk_add_f32 v[136:137], v[130:131], v[132:133]
	s_waitcnt vmcnt(11)
	v_lshlrev_b32_e32 v179, 16, v147
	v_pk_add_f32 v[134:135], v[134:135], v[136:137]
	v_lshlrev_b32_e32 v178, 16, v146
	v_and_b32_e32 v181, 0xffff0000, v147
	v_and_b32_e32 v180, 0xffff0000, v146
	v_add_f32_e32 v134, 0, v134
	v_pk_add_f32 v[136:137], v[178:179], v[180:181]
	v_add_f32_e32 v174, v134, v135
	s_waitcnt vmcnt(10)
	v_lshlrev_b32_e32 v134, 16, v148
	v_and_b32_e32 v135, 0xffff0000, v148
	v_lshlrev_b32_e32 v166, 16, v149
	v_and_b32_e32 v167, 0xffff0000, v149
	s_waitcnt vmcnt(9)
	v_and_b32_e32 v193, 0xffff0000, v150
	v_pk_add_f32 v[136:137], v[136:137], v[136:137] op_sel:[0,1] op_sel_hi:[1,0]
	v_add_f32_e32 v188, v134, v135
	v_add_f32_e32 v184, v166, v167
	v_lshlrev_b32_e32 v175, 16, v150
	v_lshlrev_b32_e32 v189, 16, v151
	v_and_b32_e32 v185, 0xffff0000, v151
	v_mov_b32_e32 v137, v193
	v_pk_add_f32 v[136:137], v[174:175], v[136:137]
	v_pk_add_f32 v[168:169], v[188:189], v[184:185]
	s_waitcnt vmcnt(8)
	v_lshlrev_b32_e32 v171, 16, v153
	v_lshlrev_b32_e32 v170, 16, v152
	v_and_b32_e32 v211, 0xffff0000, v153
	v_and_b32_e32 v210, 0xffff0000, v152
	v_pk_add_f32 v[194:195], v[136:137], v[168:169]
	v_pk_add_f32 v[212:213], v[170:171], v[210:211]
	s_waitcnt vmcnt(7)
	v_lshlrev_b32_e32 v182, 16, v154
	v_and_b32_e32 v183, 0xffff0000, v154
	v_lshlrev_b32_e32 v186, 16, v155
	v_and_b32_e32 v187, 0xffff0000, v155
	s_waitcnt vmcnt(6)
	v_lshlrev_b32_e32 v190, 16, v156
	v_and_b32_e32 v191, 0xffff0000, v156
	v_pk_add_f32 v[194:195], v[194:195], v[194:195] op_sel:[0,1] op_sel_hi:[1,0]
	v_pk_add_f32 v[212:213], v[212:213], v[212:213] op_sel:[0,1] op_sel_hi:[1,0]
	v_add_f32_e32 v168, v182, v183
	v_add_f32_e32 v136, v186, v187
	v_lshlrev_b32_e32 v169, 16, v157
	v_and_b32_e32 v137, 0xffff0000, v157
	s_cmp_ge_i32 s1, s30
	s_cbranch_scc1 .Lp6_nopf
	s_add_i32 s98, s0, s1
	s_ashr_i32 s99, s98, 31
	s_lshl_b64 s[98:99], s[98:99], 12
	v_lshl_add_u64 v[244:245], v[162:163], 0, s[98:99]
	global_load_dwordx2 v[142:143], v[244:245], off
	global_load_dwordx2 v[144:145], v[244:245], off offset:512
	global_load_dwordx2 v[146:147], v[244:245], off offset:1024
	global_load_dwordx2 v[148:149], v[244:245], off offset:1536
	global_load_dwordx2 v[150:151], v[244:245], off offset:2048
	global_load_dwordx2 v[152:153], v[244:245], off offset:2560
	global_load_dwordx2 v[154:155], v[244:245], off offset:3072
	global_load_dwordx2 v[156:157], v[244:245], off offset:3584
